# gate/up GEMM unit top: the two compiler vmcnt(0) drains (before the slot-table lookup and after the next unit's slot-list DMA) relaxed to vmcnt(8): bias loads always have 8 younger stores
# speedup vs baseline: 1.0005x; 1.0005x over previous
;     __device__ __forceinline__ bool next(int i, pg8::Unit& u) const {
;         const int MT = tb[NEXP]; int pm, pn;
;         if (G == 256) { const int x = bx & 7, j = bx >> 3, s = i * 8 + x; pm = s * GM + j / NT; pn = j % NT; }
;         else { const int L = i * G + bx; pm = L / NT; pn = L % NT; }
;         if (pm >= MT) return false;
;         const int e = tb[128 + pm];
;         int rows = tb[40 + e] - 256 * (pm - tb[e]); rows = rows > 256 ? 256 : rows;
;         u.pm = __builtin_amdgcn_readfirstlane(pm); u.pn = __builtin_amdgcn_readfirstlane(pn); u.pb = __builtin_amdgcn_readfirstlane(e * NT + pn); u.aux = __builtin_amdgcn_readfirstlane(e); u.rows = __builtin_amdgcn_readfirstlane(rows); u.lt = __builtin_amdgcn_readfirstlane(pm - tb[e]);
;         return true;
;     }
.LBB0_1085:
	s_waitcnt lgkmcnt(0)
	v_cmp_ge_i32_e64 s[4:5], s6, v0
	v_cmp_lt_i32_e64 s[8:9], s6, v0
	s_and_b64 vcc, exec, s[4:5]
	s_mov_b32 s68, s58
	s_mov_b32 s63, s90
	s_cbranch_vccnz .LBB0_1087
	s_lshl_b32 s12, s6, 2
	v_readlane_b32 s2, v253, 53
	s_add_i32 s12, s2, s12
	v_mov_b32_e32 v0, s12
	ds_read_b32 v0, v0 offset:512
	s_ashr_i32 s12, s7, 31
	s_lshr_b32 s12, s12, 29
	s_add_i32 s12, s7, s12
	s_and_b32 s12, s12, -8
	s_waitcnt vmcnt(8) lgkmcnt(0)
	v_lshlrev_b32_e32 v130, 2, v0
	v_add_u32_e32 v130, s2, v130
	ds_read2_b32 v[130:131], v130 offset1:40
	s_sub_i32 s63, s7, s12
	v_lshlrev_b32_e32 v132, 3, v0
	v_add_u32_e32 v132, s63, v132
	v_readfirstlane_b32 s68, v0
	v_readfirstlane_b32 s36, v132
	s_waitcnt lgkmcnt(0)
	v_subrev_u32_e32 v132, s6, v130
	v_lshlrev_b32_e32 v132, 8, v132
	v_add_u32_e32 v131, v132, v131
	v_min_i32_e32 v131, 0x100, v131
	v_sub_u32_e32 v0, s6, v130
	v_readfirstlane_b32 s92, v131
	v_readfirstlane_b32 s64, v0
	s_mov_b32 s93, s6
	s_mov_b32 s20, s68
	s_mov_b32 s74, s63

; #define PG8_GDMA(u, par) do { int gl_ = lane; asm volatile("" : "+v"(gl_));        \
;         if (wid < 2) __builtin_amdgcn_global_load_lds((const unsigned*)((const char*)gslot + ((size_t)(u).aux * GCAP + (size_t)(u).lt * 256) * 8 + (size_t)(wid * 64 + gl_) * 16), \
;         (PG8_LAS unsigned*)(gtab + (par) * 2048 + wid * 1024), 16, 0, 0); } while (0)
; #define PG8_GREAD(dst, u, par) do { _Pragma("unroll") for (int h_ = 0; h_ < 2; ++h_) _Pragma("unroll") for (int i_ = 0; i_ < 2; ++i_) { const int rl_ = 128 * h_ + grl[i_]; \
;         const int tk_ = *(const PG8_LAS int*)(gtab + (par) * 2048 + rl_ * 8); const unsigned tok_ = (rl_ < (u).rows) ? ((unsigned)tk_ >> 2) : 0u; dst[h_][i_] = tok_ * (unsigned)(K * 2) + gcb[i_]; } } while (0)
; template <class Epi, class Sched, bool ALIGN_EPI = false, bool SP2 = false, bool GATHER = false>
; __device__ __forceinline__ void gemm_phase(PG8_LAS unsigned char* lds, const Gemm g, const Sched& S, const Epi& E, const int2* gslot = nullptr, PG8_LAS unsigned char* gtab = nullptr) {
;     ...
;         const bool has_next = S.next(ui + 1, nxt);
;         if constexpr (GATHER) { if (has_next) PG8_GDMA(nxt, (ui + 1) & 1); }
;         const char* nA = (has_next && !GATHER) ? (const char*)g.A + (size_t)nxt.pm * tstep : cA; const char* nB = has_next ? (const char*)g.Bt + (size_t)nxt.pb * tstep : cB;
;         for (int t = 0; t < nt; t += 2) {
;             const bool last = (t == nt - 2);
;             const char* a1 = cA + (size_t)(t + 1) * kstep;
;             const char* a2 = last ? nA : cA + (size_t)(t + 2) * kstep; const char* b2 = last ? nB : cB + (size_t)(t + 2) * kstep;
;             const char* a3 = a2 + kstep; const char* b3 = b2 + kstep;
;             if (last && has_next) S.a_ready(nxt);
;             if constexpr (GATHER) { if (last) { if (has_next) { PG8_GREAD(vN, nxt, (ui + 1) & 1); } else { _Pragma("unroll") for (int h_ = 0; h_ < 2; ++h_) _Pragma("unroll") for (int i_ = 0; i_ < 2; ++i_) vN[h_][i_] = vC[h_][i_]; } } }
;             unsigned vS[2][2];
; #pragma unroll
;             for (int h_ = 0; h_ < 2; ++h_)
; #pragma unroll
;                 for (int i_ = 0; i_ < 2; ++i_) vS[h_][i_] = (GATHER && last) ? vN[h_][i_] : vC[h_][i_];
.LBB0_1091:
	s_add_u32 s21, s10, 0x100
	s_addc_u32 s37, s11, 0
	s_lshl_b32 s8, s91, 11
	s_and_b32 s8, s8, 0x800
	s_add_i32 s65, s8, 0
	v_mov_b32_e32 v157, v1
	v_mov_b32_e32 v159, v1
	s_add_i32 s65, s65, 0x21400
	v_cmp_gt_i32_e64 s[8:9], s92, v169
	v_cmp_gt_i32_e64 s[10:11], s92, v171
	v_cmp_gt_i32_e64 s[12:13], s92, v175
	v_cmp_gt_i32_e64 s[14:15], s92, v177
	s_waitcnt vmcnt(8)
	v_lshl_add_u64 v[130:131], s[30:31], 0, v[158:159]
	v_lshl_add_u64 v[132:133], s[30:31], 0, v[156:157]
	s_mov_b32 s69, -2
	s_mov_b64 s[60:61], 0
	s_branch .LBB0_1094
